# MoE combine loop: the 8 loop-invariant gain loads hoisted out of the token loop (were reloaded and waited with the preceding store 4x per token)
# speedup vs baseline: 1.0119x; 1.0062x over previous
; __device__ __forceinline__ u32x4 pack8(f32x4 v0, f32x4 v1) { u32x4 w; w.x = cvt_pk_bf16(v0[0], v0[1]); w.y = cvt_pk_bf16(v0[2], v0[3]); w.z = cvt_pk_bf16(v1[0], v1[1]); w.w = cvt_pk_bf16(v1[2], v1[3]); return w; }
; __device__ __forceinline__ void unpack8(u32x4 w, f32x4& v0, f32x4& v1) { v0 = (f32x4){bf_lo(w.x), bf_hi(w.x), bf_lo(w.y), bf_hi(w.y)}; v1 = (f32x4){bf_lo(w.z), bf_hi(w.z), bf_lo(w.w), bf_hi(w.w)}; }
; __global__ void __launch_bounds__(NWAVES * 64, 2) mk_fwd(Args a) {
;     ...
;             { for (int tok = gw; tok < NT; tok += ngw) { const int d0 = tokdest[tok * 2], d1 = tokdest[tok * 2 + 1]; float sq = 0.f;
; #pragma unroll
;                   for (int j = 0; j < 4; ++j) { const size_t o = (size_t)tok * DM + (lane + 64 * j) * 8; f32x4 x0, x1, p0, p1, q0, q1; epi::unpack8(*(const u32x4*)(XR + o), x0, x1);
;                       epi::unpack8(*(const u32x4*)(YB + (size_t)d0 * DM + (lane + 64 * j) * 8), p0, p1); epi::unpack8(*(const u32x4*)(YB + (size_t)d1 * DM + (lane + 64 * j) * 8), q0, q1);
;                       x0 += p0 + q0; x1 += p1 + q1;
; #pragma unroll
;                       for (int dd = 0; dd < 2; ++dd) { const int d = dd ? d1 : d0; if (d >= 16384) {
; #pragma unroll
;                           for (int s = 0; s < 3; ++s) { epi::unpack8(*(const u32x4*)((const bf16_t*)(ws + wsm::YBX) + ((size_t)s * 2048 + (d - 16384)) * DM + (lane + 64 * j) * 8), p0, p1); x0 += p0; x1 += p1; } } } *(u32x4*)(XR + o) = epi::pack8(x0, x1);
;                       const float* gp = a.in[28] + DM + (lane + 64 * j) * 8; const f32x4 y0 = x0 * *(const f32x4*)gp, y1 = x1 * *(const f32x4*)(gp + 4);
.LBB0_2409:
	s_cmpk_gt_i32 s96, 0x1fff
	s_cbranch_scc1 .LBB0_2430
	v_lshlrev_b32_e32 v1, 3, v194
	s_add_u32 s4, s52, 0x5b200000
	v_readlane_b32 s60, v247, 36
	s_addc_u32 s5, s53, 0
	v_readlane_b32 s68, v247, 44
	v_readlane_b32 s69, v247, 45
	s_waitcnt vmcnt(0)
	v_lshlrev_b32_e32 v2, 4, v194
	s_waitcnt lgkmcnt(0)
	v_mov_b32_e32 v3, 0
	v_or_b32_e32 v16, 0x200, v1
	s_mov_b64 s[12:13], s[68:69]
	v_lshl_add_u64 v[4:5], s[4:5], 0, v[2:3]
	v_or_b32_e32 v18, 0x400, v1
	v_lshl_add_u64 v[14:15], s[14:15], 0, v[2:3]
	v_lshlrev_b32_e32 v2, 1, v16
	s_add_u32 s6, s12, 0x2000
	v_lshlrev_b32_e32 v8, 2, v16
	v_or_b32_e32 v1, 0x600, v1
	v_lshl_add_u64 v[16:17], s[4:5], 0, v[2:3]
	v_lshlrev_b32_e32 v2, 1, v18
	s_addc_u32 s7, s13, 0
	v_lshlrev_b32_e32 v10, 2, v18
	v_lshl_add_u64 v[18:19], s[4:5], 0, v[2:3]
	v_lshlrev_b32_e32 v2, 1, v1
	s_ashr_i32 s97, s96, 31
	v_lshl_add_u64 v[20:21], s[4:5], 0, v[2:3]
	s_lshl_b64 s[4:5], s[96:97], 3
	s_add_u32 s3, s4, 0x54000
	s_addc_u32 s34, s5, 0
	s_lshl_b64 s[4:5], s[96:97], 12
	v_mov_b32_e32 v23, s5
	v_readlane_b32 s5, v247, 0
	v_lshlrev_b32_e32 v6, 5, v194
	v_mov_b32_e32 v7, v3
	v_mov_b32_e32 v9, v3
	v_mov_b32_e32 v11, v3
	v_lshlrev_b32_e32 v12, 2, v1
	v_mov_b32_e32 v13, v3
	s_ashr_i32 s59, s58, 31
	v_lshl_or_b32 v22, v194, 4, s4
	s_lshl_b32 s4, s2, 4
	s_lshl_b32 s5, s5, 1
	v_mbcnt_lo_u32_b32 v1, -1, 0
	s_mov_b32 s13, 0
	v_cmp_eq_u32_e64 s[0:1], 0, v194
	v_lshl_add_u64 v[6:7], s[6:7], 0, v[6:7]
	v_lshl_add_u64 v[8:9], s[6:7], 0, v[8:9]
	v_lshl_add_u64 v[10:11], s[6:7], 0, v[10:11]
	v_lshl_add_u64 v[12:13], s[6:7], 0, v[12:13]
	s_lshl_b64 s[14:15], s[58:59], 3
	s_lshl_b64 s[16:17], s[58:59], 12
	s_add_i32 s18, s4, s5
	s_lshl_b32 s35, s33, 4
	s_mov_b64 s[20:21], 0x37e00000
	s_mov_b32 s40, 0x37e00000
	s_mov_b32 s41, 0x800000
	s_mov_b32 s44, 0x1000000
	s_mov_b32 s45, 0x3de00000
	s_mov_b64 s[22:23], 0x37e00400
	s_mov_b64 s[24:25], 0x37e00800
	s_mov_b64 s[28:29], 0x37e00c00
	v_mbcnt_hi_u32_b32 v1, -1, v1
	v_readlane_b32 s61, v247, 37
	v_readlane_b32 s62, v247, 38
	v_readlane_b32 s63, v247, 39
	v_readlane_b32 s64, v247, 40
	v_readlane_b32 s65, v247, 41
	v_readlane_b32 s66, v247, 42
	v_readlane_b32 s67, v247, 43
	v_readlane_b32 s70, v247, 46
	v_readlane_b32 s71, v247, 47
	v_readlane_b32 s72, v247, 48
	v_readlane_b32 s73, v247, 49
	v_readlane_b32 s74, v247, 50
	v_readlane_b32 s75, v247, 51
	global_load_dwordx4 v[100:103], v[6:7], off
	global_load_dwordx4 v[104:107], v[6:7], off offset:16
	global_load_dwordx4 v[108:111], v[8:9], off
	global_load_dwordx4 v[112:115], v[8:9], off offset:16
	global_load_dwordx4 v[116:119], v[10:11], off
	global_load_dwordx4 v[120:123], v[10:11], off offset:16
	global_load_dwordx4 v[124:127], v[12:13], off
	global_load_dwordx4 v[128:131], v[12:13], off offset:16
	s_branch .LBB0_2412

; __device__ __forceinline__ u32x4 pack8(f32x4 v0, f32x4 v1) { u32x4 w; w.x = cvt_pk_bf16(v0[0], v0[1]); w.y = cvt_pk_bf16(v0[2], v0[3]); w.z = cvt_pk_bf16(v1[0], v1[1]); w.w = cvt_pk_bf16(v1[2], v1[3]); return w; }
; __device__ __forceinline__ void unpack8(u32x4 w, f32x4& v0, f32x4& v1) { v0 = (f32x4){bf_lo(w.x), bf_hi(w.x), bf_lo(w.y), bf_hi(w.y)}; v1 = (f32x4){bf_lo(w.z), bf_hi(w.z), bf_lo(w.w), bf_hi(w.w)}; }
; __global__ void __launch_bounds__(NWAVES * 64, 2) mk_fwd(Args a) {
;     ...
;                   for (int j = 0; j < 4; ++j) { const size_t o = (size_t)tok * DM + (lane + 64 * j) * 8; f32x4 x0, x1, p0, p1, q0, q1; epi::unpack8(*(const u32x4*)(XR + o), x0, x1);
;                       epi::unpack8(*(const u32x4*)(YB + (size_t)d0 * DM + (lane + 64 * j) * 8), p0, p1); epi::unpack8(*(const u32x4*)(YB + (size_t)d1 * DM + (lane + 64 * j) * 8), q0, q1);
;                       x0 += p0 + q0; x1 += p1 + q1;
; #pragma unroll
;                       for (int dd = 0; dd < 2; ++dd) { const int d = dd ? d1 : d0; if (d >= 16384) {
; #pragma unroll
;                           for (int s = 0; s < 3; ++s) { epi::unpack8(*(const u32x4*)((const bf16_t*)(ws + wsm::YBX) + ((size_t)s * 2048 + (d - 16384)) * DM + (lane + 64 * j) * 8), p0, p1); x0 += p0; x1 += p1; } } } *(u32x4*)(XR + o) = epi::pack8(x0, x1);
;                       const float* gp = a.in[28] + DM + (lane + 64 * j) * 8; const f32x4 y0 = x0 * *(const f32x4*)gp, y1 = x1 * *(const f32x4*)(gp + 4);
.LBB0_2416:
	v_lshl_add_u64 v[34:35], v[24:25], 0, s[20:21]
	v_cvt_pk_bf16_f32 v42, v28, v29
	v_cvt_pk_bf16_f32 v43, v26, v27
	v_cvt_pk_bf16_f32 v44, v32, v33
	v_cvt_pk_bf16_f32 v45, v30, v31
	global_store_dwordx4 v[34:35], v[42:45], off
	s_nop 1
	v_mov_b32_e32 v42, v100
	v_mov_b32_e32 v43, v101
	v_mov_b32_e32 v44, v102
	v_mov_b32_e32 v45, v103
	s_nop 0
	s_nop 1
	v_mov_b32_e32 v46, v104
	v_mov_b32_e32 v47, v105
	v_mov_b32_e32 v48, v106
	v_mov_b32_e32 v49, v107
	v_cndmask_b32_e64 v2, 0, 1, s[6:7]
	v_cmp_ne_u32_e64 s[4:5], 1, v2
	s_nop 0
	v_pk_mul_f32 v[34:35], v[26:27], v[44:45]
	v_pk_mul_f32 v[42:43], v[28:29], v[42:43]
	s_nop 0
	v_pk_mul_f32 v[44:45], v[32:33], v[46:47]
	v_cvt_pk_bf16_f32 v42, v42, v43
	v_cvt_pk_bf16_f32 v43, v34, v35
	v_add_co_u32_e32 v34, vcc, s45, v24
	v_pk_mul_f32 v[48:49], v[30:31], v[48:49]
	s_nop 0
	v_addc_co_u32_e32 v35, vcc, 0, v25, vcc
	v_cvt_pk_bf16_f32 v44, v44, v45
	v_cvt_pk_bf16_f32 v45, v48, v49
	global_store_dwordx4 v[34:35], v[42:45], off
	global_load_dwordx4 v[46:49], v[36:37], off offset:1024
	s_nop 0
	global_load_dwordx4 v[42:45], v[38:39], off offset:1024
	global_load_dwordx4 v[50:53], v[40:41], off offset:1024
	s_andn2_b64 vcc, exec, s[6:7]
	s_waitcnt vmcnt(2)
	v_lshlrev_b32_e32 v54, 16, v46
	s_waitcnt vmcnt(1)
	v_lshlrev_b32_e32 v58, 16, v42
	v_and_b32_e32 v59, 0xffff0000, v42
	v_lshlrev_b32_e32 v42, 16, v43
	v_and_b32_e32 v43, 0xffff0000, v43
	v_lshlrev_b32_e32 v60, 16, v44
	v_and_b32_e32 v61, 0xffff0000, v44
	v_lshlrev_b32_e32 v44, 16, v45
	v_and_b32_e32 v45, 0xffff0000, v45
	s_waitcnt vmcnt(0)
	v_lshlrev_b32_e32 v62, 16, v50
	v_and_b32_e32 v63, 0xffff0000, v50
	v_lshlrev_b32_e32 v50, 16, v51
	v_and_b32_e32 v51, 0xffff0000, v51
	v_lshlrev_b32_e32 v64, 16, v52
	v_and_b32_e32 v65, 0xffff0000, v52
	v_lshlrev_b32_e32 v52, 16, v53
	v_and_b32_e32 v53, 0xffff0000, v53
	v_and_b32_e32 v55, 0xffff0000, v46
	v_lshlrev_b32_e32 v46, 16, v47
	v_and_b32_e32 v47, 0xffff0000, v47
	v_lshlrev_b32_e32 v56, 16, v48
	v_and_b32_e32 v57, 0xffff0000, v48
	v_lshlrev_b32_e32 v48, 16, v49
	v_and_b32_e32 v49, 0xffff0000, v49
	v_pk_add_f32 v[58:59], v[58:59], v[62:63]
	v_pk_add_f32 v[42:43], v[42:43], v[50:51]
	v_pk_add_f32 v[50:51], v[60:61], v[64:65]
	v_pk_add_f32 v[52:53], v[44:45], v[52:53]
	v_pk_add_f32 v[42:43], v[42:43], v[46:47]
	v_pk_add_f32 v[44:45], v[58:59], v[54:55]
	v_pk_add_f32 v[46:47], v[52:53], v[48:49]
	v_pk_add_f32 v[48:49], v[50:51], v[56:57]
	s_cbranch_vccnz .LBB0_2418
	s_add_i32 s12, s36, 0xffffc000
	s_lshl_b64 s[6:7], s[12:13], 12
	v_lshl_add_u64 v[58:59], v[16:17], 0, s[6:7]
	v_add_co_u32_e32 v54, vcc, s41, v58
	global_load_dwordx4 v[50:53], v[58:59], off
	s_nop 0
	v_addc_co_u32_e32 v55, vcc, 0, v59, vcc
	global_load_dwordx4 v[54:57], v[54:55], off
	v_add_co_u32_e32 v58, vcc, s44, v58
	s_waitcnt vmcnt(1)
	v_lshlrev_b32_e32 v62, 16, v50
	v_addc_co_u32_e32 v59, vcc, 0, v59, vcc
	global_load_dwordx4 v[58:61], v[58:59], off
	v_and_b32_e32 v63, 0xffff0000, v50
	v_lshlrev_b32_e32 v50, 16, v51
	v_and_b32_e32 v51, 0xffff0000, v51
	v_lshlrev_b32_e32 v64, 16, v52
	v_and_b32_e32 v65, 0xffff0000, v52
	v_lshlrev_b32_e32 v52, 16, v53
	v_and_b32_e32 v53, 0xffff0000, v53
	v_pk_add_f32 v[42:43], v[42:43], v[50:51]
	v_pk_add_f32 v[44:45], v[44:45], v[62:63]
	v_pk_add_f32 v[46:47], v[46:47], v[52:53]
	v_pk_add_f32 v[48:49], v[48:49], v[64:65]
	s_waitcnt vmcnt(1)
	v_lshlrev_b32_e32 v50, 16, v54
	v_and_b32_e32 v51, 0xffff0000, v54
	v_lshlrev_b32_e32 v52, 16, v55
	v_and_b32_e32 v53, 0xffff0000, v55
	v_lshlrev_b32_e32 v54, 16, v56
	v_and_b32_e32 v55, 0xffff0000, v56
	v_lshlrev_b32_e32 v56, 16, v57
	v_and_b32_e32 v57, 0xffff0000, v57
	v_pk_add_f32 v[44:45], v[44:45], v[50:51]
	v_pk_add_f32 v[42:43], v[42:43], v[52:53]
	v_pk_add_f32 v[48:49], v[48:49], v[54:55]
	v_pk_add_f32 v[46:47], v[46:47], v[56:57]
	s_waitcnt vmcnt(0)
	v_lshlrev_b32_e32 v62, 16, v58
	v_and_b32_e32 v63, 0xffff0000, v58
	v_lshlrev_b32_e32 v58, 16, v59
	v_and_b32_e32 v59, 0xffff0000, v59
	v_lshlrev_b32_e32 v64, 16, v60
	v_and_b32_e32 v65, 0xffff0000, v60
	v_lshlrev_b32_e32 v60, 16, v61
	v_and_b32_e32 v61, 0xffff0000, v61
	v_pk_add_f32 v[42:43], v[42:43], v[58:59]
	v_pk_add_f32 v[44:45], v[44:45], v[62:63]
	v_pk_add_f32 v[46:47], v[46:47], v[60:61]
	v_pk_add_f32 v[48:49], v[48:49], v[64:65]

; __device__ __forceinline__ u32x4 pack8(f32x4 v0, f32x4 v1) { u32x4 w; w.x = cvt_pk_bf16(v0[0], v0[1]); w.y = cvt_pk_bf16(v0[2], v0[3]); w.z = cvt_pk_bf16(v1[0], v1[1]); w.w = cvt_pk_bf16(v1[2], v1[3]); return w; }
; __device__ __forceinline__ void unpack8(u32x4 w, f32x4& v0, f32x4& v1) { v0 = (f32x4){bf_lo(w.x), bf_hi(w.x), bf_lo(w.y), bf_hi(w.y)}; v1 = (f32x4){bf_lo(w.z), bf_hi(w.z), bf_lo(w.w), bf_hi(w.w)}; }
; __global__ void __launch_bounds__(NWAVES * 64, 2) mk_fwd(Args a) {
;     ...
;                   for (int j = 0; j < 4; ++j) { const size_t o = (size_t)tok * DM + (lane + 64 * j) * 8; f32x4 x0, x1, p0, p1, q0, q1; epi::unpack8(*(const u32x4*)(XR + o), x0, x1);
;                       epi::unpack8(*(const u32x4*)(YB + (size_t)d0 * DM + (lane + 64 * j) * 8), p0, p1); epi::unpack8(*(const u32x4*)(YB + (size_t)d1 * DM + (lane + 64 * j) * 8), q0, q1);
;                       x0 += p0 + q0; x1 += p1 + q1;
; #pragma unroll
;                       for (int dd = 0; dd < 2; ++dd) { const int d = dd ? d1 : d0; if (d >= 16384) {
; #pragma unroll
;                           for (int s = 0; s < 3; ++s) { epi::unpack8(*(const u32x4*)((const bf16_t*)(ws + wsm::YBX) + ((size_t)s * 2048 + (d - 16384)) * DM + (lane + 64 * j) * 8), p0, p1); x0 += p0; x1 += p1; } } } *(u32x4*)(XR + o) = epi::pack8(x0, x1);
;                       const float* gp = a.in[28] + DM + (lane + 64 * j) * 8; const f32x4 y0 = x0 * *(const f32x4*)gp, y1 = x1 * *(const f32x4*)(gp + 4);
.LBB0_2420:
	v_lshl_add_u64 v[54:55], v[24:25], 0, s[22:23]
	v_cvt_pk_bf16_f32 v50, v44, v45
	v_cvt_pk_bf16_f32 v51, v42, v43
	v_cvt_pk_bf16_f32 v52, v48, v49
	v_cvt_pk_bf16_f32 v53, v46, v47
	global_store_dwordx4 v[54:55], v[50:53], off
	s_nop 1
	v_mov_b32_e32 v50, v108
	v_mov_b32_e32 v51, v109
	v_mov_b32_e32 v52, v110
	v_mov_b32_e32 v53, v111
	s_nop 0
	s_nop 1
	v_mov_b32_e32 v54, v112
	v_mov_b32_e32 v55, v113
	v_mov_b32_e32 v56, v114
	v_mov_b32_e32 v57, v115
	s_and_b64 vcc, exec, s[4:5]
	s_nop 0
	v_pk_mul_f32 v[52:53], v[42:43], v[52:53]
	v_pk_mul_f32 v[50:51], v[44:45], v[50:51]
	s_nop 0
	v_pk_mul_f32 v[56:57], v[46:47], v[56:57]
	v_pk_mul_f32 v[54:55], v[48:49], v[54:55]
	v_cvt_pk_bf16_f32 v50, v50, v51
	v_cvt_pk_bf16_f32 v51, v52, v53
	s_nop 0
	v_cvt_pk_bf16_f32 v52, v54, v55
	v_cvt_pk_bf16_f32 v53, v56, v57
	global_store_dwordx4 v[34:35], v[50:53], off offset:1024
	global_load_dwordx4 v[54:57], v[36:37], off offset:2048
	s_nop 0
	global_load_dwordx4 v[50:53], v[38:39], off offset:2048
	global_load_dwordx4 v[58:61], v[40:41], off offset:2048
	s_waitcnt vmcnt(1)
	v_lshlrev_b32_e32 v66, 16, v50
	v_and_b32_e32 v67, 0xffff0000, v50
	v_lshlrev_b32_e32 v50, 16, v51
	v_and_b32_e32 v51, 0xffff0000, v51
	v_lshlrev_b32_e32 v68, 16, v52
	v_and_b32_e32 v69, 0xffff0000, v52
	v_lshlrev_b32_e32 v52, 16, v53
	v_and_b32_e32 v53, 0xffff0000, v53
	s_waitcnt vmcnt(0)
	v_lshlrev_b32_e32 v70, 16, v58
	v_and_b32_e32 v71, 0xffff0000, v58
	v_lshlrev_b32_e32 v58, 16, v59
	v_and_b32_e32 v59, 0xffff0000, v59
	v_lshlrev_b32_e32 v72, 16, v60
	v_and_b32_e32 v73, 0xffff0000, v60
	v_lshlrev_b32_e32 v60, 16, v61
	v_and_b32_e32 v61, 0xffff0000, v61
	v_lshlrev_b32_e32 v62, 16, v54
	v_and_b32_e32 v63, 0xffff0000, v54
	v_lshlrev_b32_e32 v54, 16, v55
	v_and_b32_e32 v55, 0xffff0000, v55
	v_lshlrev_b32_e32 v64, 16, v56
	v_and_b32_e32 v65, 0xffff0000, v56
	v_lshlrev_b32_e32 v56, 16, v57
	v_and_b32_e32 v57, 0xffff0000, v57
	v_pk_add_f32 v[66:67], v[66:67], v[70:71]
	v_pk_add_f32 v[50:51], v[50:51], v[58:59]
	v_pk_add_f32 v[58:59], v[68:69], v[72:73]
	v_pk_add_f32 v[60:61], v[52:53], v[60:61]
	v_pk_add_f32 v[50:51], v[50:51], v[54:55]
	v_pk_add_f32 v[52:53], v[66:67], v[62:63]
	v_pk_add_f32 v[54:55], v[60:61], v[56:57]
	v_pk_add_f32 v[56:57], v[58:59], v[64:65]
	s_cbranch_vccnz .LBB0_2422
	s_add_i32 s12, s36, 0xffffc000
	s_lshl_b64 s[38:39], s[12:13], 12
	v_lshl_add_u64 v[66:67], v[18:19], 0, s[38:39]
	v_add_co_u32_e32 v62, vcc, s41, v66
	global_load_dwordx4 v[58:61], v[66:67], off
	s_nop 0
	v_addc_co_u32_e32 v63, vcc, 0, v67, vcc
	global_load_dwordx4 v[62:65], v[62:63], off
	v_add_co_u32_e32 v66, vcc, s44, v66
	s_waitcnt vmcnt(1)
	v_lshlrev_b32_e32 v70, 16, v58
	v_addc_co_u32_e32 v67, vcc, 0, v67, vcc
	global_load_dwordx4 v[66:69], v[66:67], off
	v_and_b32_e32 v71, 0xffff0000, v58
	v_lshlrev_b32_e32 v58, 16, v59
	v_and_b32_e32 v59, 0xffff0000, v59
	v_lshlrev_b32_e32 v72, 16, v60
	v_and_b32_e32 v73, 0xffff0000, v60
	v_lshlrev_b32_e32 v60, 16, v61
	v_and_b32_e32 v61, 0xffff0000, v61
	v_pk_add_f32 v[50:51], v[50:51], v[58:59]
	v_pk_add_f32 v[52:53], v[52:53], v[70:71]
	v_pk_add_f32 v[54:55], v[54:55], v[60:61]
	v_pk_add_f32 v[56:57], v[56:57], v[72:73]
	s_waitcnt vmcnt(1)
	v_lshlrev_b32_e32 v58, 16, v62
	v_and_b32_e32 v59, 0xffff0000, v62
	v_lshlrev_b32_e32 v60, 16, v63
	v_and_b32_e32 v61, 0xffff0000, v63
	v_lshlrev_b32_e32 v62, 16, v64
	v_and_b32_e32 v63, 0xffff0000, v64
	v_lshlrev_b32_e32 v64, 16, v65
	v_and_b32_e32 v65, 0xffff0000, v65
	v_pk_add_f32 v[52:53], v[52:53], v[58:59]
	v_pk_add_f32 v[50:51], v[50:51], v[60:61]
	v_pk_add_f32 v[56:57], v[56:57], v[62:63]
	v_pk_add_f32 v[54:55], v[54:55], v[64:65]
	s_waitcnt vmcnt(0)
	v_lshlrev_b32_e32 v70, 16, v66
	v_and_b32_e32 v71, 0xffff0000, v66
	v_lshlrev_b32_e32 v66, 16, v67
	v_and_b32_e32 v67, 0xffff0000, v67
	v_lshlrev_b32_e32 v72, 16, v68
	v_and_b32_e32 v73, 0xffff0000, v68
	v_lshlrev_b32_e32 v68, 16, v69
	v_and_b32_e32 v69, 0xffff0000, v69
	v_pk_add_f32 v[50:51], v[50:51], v[66:67]
	v_pk_add_f32 v[52:53], v[52:53], v[70:71]
	v_pk_add_f32 v[54:55], v[54:55], v[68:69]
	v_pk_add_f32 v[56:57], v[56:57], v[72:73]

; __device__ __forceinline__ u32x4 pack8(f32x4 v0, f32x4 v1) { u32x4 w; w.x = cvt_pk_bf16(v0[0], v0[1]); w.y = cvt_pk_bf16(v0[2], v0[3]); w.z = cvt_pk_bf16(v1[0], v1[1]); w.w = cvt_pk_bf16(v1[2], v1[3]); return w; }
; __device__ __forceinline__ void unpack8(u32x4 w, f32x4& v0, f32x4& v1) { v0 = (f32x4){bf_lo(w.x), bf_hi(w.x), bf_lo(w.y), bf_hi(w.y)}; v1 = (f32x4){bf_lo(w.z), bf_hi(w.z), bf_lo(w.w), bf_hi(w.w)}; }
; __global__ void __launch_bounds__(NWAVES * 64, 2) mk_fwd(Args a) {
;     ...
;                   for (int j = 0; j < 4; ++j) { const size_t o = (size_t)tok * DM + (lane + 64 * j) * 8; f32x4 x0, x1, p0, p1, q0, q1; epi::unpack8(*(const u32x4*)(XR + o), x0, x1);
;                       epi::unpack8(*(const u32x4*)(YB + (size_t)d0 * DM + (lane + 64 * j) * 8), p0, p1); epi::unpack8(*(const u32x4*)(YB + (size_t)d1 * DM + (lane + 64 * j) * 8), q0, q1);
;                       x0 += p0 + q0; x1 += p1 + q1;
; #pragma unroll
;                       for (int dd = 0; dd < 2; ++dd) { const int d = dd ? d1 : d0; if (d >= 16384) {
; #pragma unroll
;                           for (int s = 0; s < 3; ++s) { epi::unpack8(*(const u32x4*)((const bf16_t*)(ws + wsm::YBX) + ((size_t)s * 2048 + (d - 16384)) * DM + (lane + 64 * j) * 8), p0, p1); x0 += p0; x1 += p1; } } } *(u32x4*)(XR + o) = epi::pack8(x0, x1);
;                       const float* gp = a.in[28] + DM + (lane + 64 * j) * 8; const f32x4 y0 = x0 * *(const f32x4*)gp, y1 = x1 * *(const f32x4*)(gp + 4);
.LBB0_2424:
	v_lshl_add_u64 v[62:63], v[24:25], 0, s[24:25]
	v_cvt_pk_bf16_f32 v58, v52, v53
	v_cvt_pk_bf16_f32 v59, v50, v51
	v_cvt_pk_bf16_f32 v60, v56, v57
	v_cvt_pk_bf16_f32 v61, v54, v55
	global_store_dwordx4 v[62:63], v[58:61], off
	s_nop 1
	v_mov_b32_e32 v58, v116
	v_mov_b32_e32 v59, v117
	v_mov_b32_e32 v60, v118
	v_mov_b32_e32 v61, v119
	s_nop 0
	s_nop 1
	v_mov_b32_e32 v62, v120
	v_mov_b32_e32 v63, v121
	v_mov_b32_e32 v64, v122
	v_mov_b32_e32 v65, v123
	s_and_b64 vcc, exec, s[4:5]
	s_nop 0
	v_pk_mul_f32 v[60:61], v[50:51], v[60:61]
	v_pk_mul_f32 v[58:59], v[52:53], v[58:59]
	s_nop 0
	v_pk_mul_f32 v[64:65], v[54:55], v[64:65]
	v_pk_mul_f32 v[62:63], v[56:57], v[62:63]
	v_cvt_pk_bf16_f32 v58, v58, v59
	v_cvt_pk_bf16_f32 v59, v60, v61
	s_nop 0
	v_cvt_pk_bf16_f32 v60, v62, v63
	v_cvt_pk_bf16_f32 v61, v64, v65
	global_store_dwordx4 v[34:35], v[58:61], off offset:2048
	global_load_dwordx4 v[62:65], v[36:37], off offset:3072
	s_nop 0
	global_load_dwordx4 v[36:39], v[38:39], off offset:3072
	s_nop 0
	global_load_dwordx4 v[58:61], v[40:41], off offset:3072
	s_waitcnt vmcnt(1)
	v_lshlrev_b32_e32 v68, 16, v36
	v_and_b32_e32 v69, 0xffff0000, v36
	v_lshlrev_b32_e32 v36, 16, v37
	v_and_b32_e32 v37, 0xffff0000, v37
	v_lshlrev_b32_e32 v70, 16, v38
	v_and_b32_e32 v71, 0xffff0000, v38
	v_lshlrev_b32_e32 v38, 16, v39
	v_and_b32_e32 v39, 0xffff0000, v39
	s_waitcnt vmcnt(0)
	v_lshlrev_b32_e32 v72, 16, v58
	v_and_b32_e32 v73, 0xffff0000, v58
	v_lshlrev_b32_e32 v58, 16, v59
	v_and_b32_e32 v59, 0xffff0000, v59
	v_lshlrev_b32_e32 v74, 16, v60
	v_and_b32_e32 v75, 0xffff0000, v60
	v_lshlrev_b32_e32 v60, 16, v61
	v_and_b32_e32 v61, 0xffff0000, v61
	v_lshlrev_b32_e32 v40, 16, v62
	v_and_b32_e32 v41, 0xffff0000, v62
	v_lshlrev_b32_e32 v62, 16, v63
	v_and_b32_e32 v63, 0xffff0000, v63
	v_lshlrev_b32_e32 v66, 16, v64
	v_and_b32_e32 v67, 0xffff0000, v64
	v_lshlrev_b32_e32 v64, 16, v65
	v_and_b32_e32 v65, 0xffff0000, v65
	v_pk_add_f32 v[68:69], v[68:69], v[72:73]
	v_pk_add_f32 v[36:37], v[36:37], v[58:59]
	v_pk_add_f32 v[58:59], v[70:71], v[74:75]
	v_pk_add_f32 v[60:61], v[38:39], v[60:61]
	v_pk_add_f32 v[38:39], v[36:37], v[62:63]
	v_pk_add_f32 v[36:37], v[68:69], v[40:41]
	v_pk_add_f32 v[40:41], v[60:61], v[64:65]
	v_pk_add_f32 v[58:59], v[58:59], v[66:67]
	s_cbranch_vccnz .LBB0_2426
	s_add_i32 s12, s36, 0xffffc000
	s_lshl_b64 s[4:5], s[12:13], 12
	v_lshl_add_u64 v[68:69], v[20:21], 0, s[4:5]
	v_add_co_u32_e32 v64, vcc, s41, v68
	global_load_dwordx4 v[60:63], v[68:69], off
	s_nop 0
	v_addc_co_u32_e32 v65, vcc, 0, v69, vcc
	global_load_dwordx4 v[64:67], v[64:65], off
	v_add_co_u32_e32 v68, vcc, s44, v68
	s_waitcnt vmcnt(1)
	v_lshlrev_b32_e32 v72, 16, v60
	v_addc_co_u32_e32 v69, vcc, 0, v69, vcc
	global_load_dwordx4 v[68:71], v[68:69], off
	v_and_b32_e32 v73, 0xffff0000, v60
	v_lshlrev_b32_e32 v60, 16, v61
	v_and_b32_e32 v61, 0xffff0000, v61
	v_lshlrev_b32_e32 v74, 16, v62
	v_and_b32_e32 v75, 0xffff0000, v62
	v_lshlrev_b32_e32 v62, 16, v63
	v_and_b32_e32 v63, 0xffff0000, v63
	v_pk_add_f32 v[38:39], v[38:39], v[60:61]
	v_pk_add_f32 v[36:37], v[36:37], v[72:73]
	v_pk_add_f32 v[40:41], v[40:41], v[62:63]
	v_pk_add_f32 v[58:59], v[58:59], v[74:75]
	s_waitcnt vmcnt(1)
	v_lshlrev_b32_e32 v60, 16, v64
	v_and_b32_e32 v61, 0xffff0000, v64
	v_lshlrev_b32_e32 v62, 16, v65
	v_and_b32_e32 v63, 0xffff0000, v65
	v_lshlrev_b32_e32 v64, 16, v66
	v_and_b32_e32 v65, 0xffff0000, v66
	v_lshlrev_b32_e32 v66, 16, v67
	v_and_b32_e32 v67, 0xffff0000, v67
	v_pk_add_f32 v[36:37], v[36:37], v[60:61]
	v_pk_add_f32 v[38:39], v[38:39], v[62:63]
	v_pk_add_f32 v[58:59], v[58:59], v[64:65]
	v_pk_add_f32 v[40:41], v[40:41], v[66:67]
	s_waitcnt vmcnt(0)
	v_lshlrev_b32_e32 v72, 16, v68
	v_and_b32_e32 v73, 0xffff0000, v68
	v_lshlrev_b32_e32 v68, 16, v69
	v_and_b32_e32 v69, 0xffff0000, v69
	v_lshlrev_b32_e32 v74, 16, v70
	v_and_b32_e32 v75, 0xffff0000, v70
	v_lshlrev_b32_e32 v70, 16, v71
	v_and_b32_e32 v71, 0xffff0000, v71
	v_pk_add_f32 v[38:39], v[38:39], v[68:69]
	v_pk_add_f32 v[36:37], v[36:37], v[72:73]
	v_pk_add_f32 v[40:41], v[40:41], v[70:71]
	v_pk_add_f32 v[58:59], v[58:59], v[74:75]

; __device__ __forceinline__ unsigned pk4_fp8(float a, float b, float c, float d) { int w = 0; w = __builtin_amdgcn_cvt_pk_fp8_f32(a, b, w, false); w = __builtin_amdgcn_cvt_pk_fp8_f32(c, d, w, true); return (unsigned)w; }
; __device__ __forceinline__ u32x4 pack8(f32x4 v0, f32x4 v1) { u32x4 w; w.x = cvt_pk_bf16(v0[0], v0[1]); w.y = cvt_pk_bf16(v0[2], v0[3]); w.z = cvt_pk_bf16(v1[0], v1[1]); w.w = cvt_pk_bf16(v1[2], v1[3]); return w; }
; __device__ __forceinline__ float sum8sq(f32x4 a, f32x4 b) { return (a[0] * a[0] + a[1] * a[1]) + (a[2] * a[2] + a[3] * a[3]) + (b[0] * b[0] + b[1] * b[1]) + (b[2] * b[2] + b[3] * b[3]); }
; __device__ __forceinline__ ss_t ss_fix(float sq) { return (ss_t)(sq * 16777216.f); }
; __device__ __forceinline__ float wave_sum(float v) {
; #pragma unroll
;     for (int o = 1; o < 64; o <<= 1) v += __shfl_xor(v, o);
;     return v;
; __global__ void __launch_bounds__(NWAVES * 64, 2) mk_fwd(Args a) {
;     ...
;                       const float* gp = a.in[28] + DM + (lane + 64 * j) * 8; const f32x4 y0 = x0 * *(const f32x4*)gp, y1 = x1 * *(const f32x4*)(gp + 4);
;                       if constexpr (F8P) *(u32x2*)((unsigned char*)x2b + o) = (u32x2){pk4_fp8(y0[0], y0[1], y0[2], y0[3]), pk4_fp8(y1[0], y1[1], y1[2], y1[3])}; else *(u32x4*)(x2b + o) = epi::pack8(y0, y1);
;                       sq += epi::sum8sq(x0, x1); }
;                   sq = wave_sum(sq); if (lane == 0) ssx2[tok] = epi::ss_fix(sq); } }
.LBB0_2428:
	v_lshl_add_u64 v[60:61], v[24:25], 0, s[28:29]
	v_mul_f32_e32 v2, v29, v29
	v_mul_f32_e32 v24, v27, v27
	v_fmac_f32_e32 v2, v28, v28
	v_fmac_f32_e32 v24, v26, v26
	v_add_f32_e32 v2, v2, v24
	v_mul_f32_e32 v24, v33, v33
	v_fmac_f32_e32 v24, v32, v32
	v_add_f32_e32 v2, v24, v2
	v_mul_f32_e32 v32, v31, v31
	v_cvt_pk_bf16_f32 v24, v36, v37
	v_cvt_pk_bf16_f32 v25, v38, v39
	v_cvt_pk_bf16_f32 v26, v58, v59
	v_cvt_pk_bf16_f32 v27, v40, v41
	global_store_dwordx4 v[60:61], v[24:27], off
	v_fmac_f32_e32 v32, v30, v30
	s_nop 1
	v_mov_b32_e32 v24, v128
	v_mov_b32_e32 v25, v129
	v_mov_b32_e32 v26, v130
	v_mov_b32_e32 v27, v131
	s_nop 1
	v_mov_b32_e32 v28, v124
	v_mov_b32_e32 v29, v125
	v_mov_b32_e32 v30, v126
	v_mov_b32_e32 v31, v127
	v_add_f32_e32 v2, v32, v2
	v_mul_f32_e32 v32, v45, v45
	v_mul_f32_e32 v33, v43, v43
	v_fmac_f32_e32 v32, v44, v44
	v_fmac_f32_e32 v33, v42, v42
	v_add_f32_e32 v32, v32, v33
	v_mul_f32_e32 v33, v49, v49
	v_fmac_f32_e32 v33, v48, v48
	v_add_f32_e32 v32, v33, v32
	v_mul_f32_e32 v33, v47, v47
	v_fmac_f32_e32 v33, v46, v46
	v_add_f32_e32 v32, v33, v32
	v_add_f32_e32 v2, v2, v32
	v_mul_f32_e32 v32, v53, v53
	v_mul_f32_e32 v33, v51, v51
	v_fmac_f32_e32 v32, v52, v52
	v_fmac_f32_e32 v33, v50, v50
	v_add_f32_e32 v32, v32, v33
	v_mul_f32_e32 v33, v57, v57
	v_fmac_f32_e32 v33, v56, v56
	v_add_f32_e32 v32, v33, v32
	v_mul_f32_e32 v33, v55, v55
	v_fmac_f32_e32 v33, v54, v54
	v_add_f32_e32 v32, v33, v32
	v_add_f32_e32 v2, v2, v32
	v_mul_f32_e32 v32, v37, v37
	v_mul_f32_e32 v33, v39, v39
	v_fmac_f32_e32 v32, v36, v36
	v_fmac_f32_e32 v33, v38, v38
	v_add_f32_e32 v32, v32, v33
	v_mul_f32_e32 v33, v59, v59
	v_fmac_f32_e32 v33, v58, v58
	v_add_f32_e32 v32, v33, v32
	v_mul_f32_e32 v33, v41, v41
	v_fmac_f32_e32 v33, v40, v40
	v_add_f32_e32 v32, v33, v32
	v_add_f32_e32 v2, v2, v32
	v_and_b32_e32 v32, 64, v1
	v_add_u32_e32 v42, 64, v32
	v_xor_b32_e32 v32, 1, v1
	v_cmp_lt_i32_e32 vcc, v32, v42
	v_xor_b32_e32 v33, 16, v1
	s_nop 0
	v_pk_mul_f32 v[30:31], v[38:39], v[30:31]
	v_cndmask_b32_e32 v32, v1, v32, vcc
	v_lshlrev_b32_e32 v32, 2, v32
	ds_bpermute_b32 v32, v32, v2
	v_pk_mul_f32 v[28:29], v[36:37], v[28:29]
	v_pk_mul_f32 v[36:37], v[58:59], v[24:25]
	v_xor_b32_e32 v24, 32, v1
	s_waitcnt lgkmcnt(0)
	v_add_f32_e32 v2, v2, v32
	v_xor_b32_e32 v32, 2, v1
	v_cmp_lt_i32_e32 vcc, v32, v42
	s_nop 1
	v_cndmask_b32_e32 v32, v1, v32, vcc
	v_lshlrev_b32_e32 v32, 2, v32
	ds_bpermute_b32 v32, v32, v2
	s_waitcnt lgkmcnt(0)
	v_add_f32_e32 v2, v2, v32
	v_xor_b32_e32 v32, 4, v1
	v_cmp_lt_i32_e32 vcc, v32, v42
	s_nop 1
	v_cndmask_b32_e32 v32, v1, v32, vcc
	v_lshlrev_b32_e32 v32, 2, v32
	ds_bpermute_b32 v32, v32, v2
	s_waitcnt lgkmcnt(0)
	v_add_f32_e32 v2, v2, v32
	v_xor_b32_e32 v32, 8, v1
	v_cmp_lt_i32_e32 vcc, v32, v42
	s_nop 1
	v_cndmask_b32_e32 v32, v1, v32, vcc
	v_lshlrev_b32_e32 v32, 2, v32
	ds_bpermute_b32 v32, v32, v2
	v_cmp_lt_i32_e32 vcc, v33, v42
	s_waitcnt lgkmcnt(0)
	v_add_f32_e32 v2, v2, v32
	v_cndmask_b32_e32 v32, v1, v33, vcc
	v_lshlrev_b32_e32 v32, 2, v32
	ds_bpermute_b32 v38, v32, v2
	v_cmp_lt_i32_e32 vcc, v24, v42
	v_pk_mul_f32 v[32:33], v[40:41], v[26:27]
	v_cvt_pk_bf16_f32 v26, v28, v29
	v_cvt_pk_bf16_f32 v27, v30, v31
	s_waitcnt lgkmcnt(0)
	v_add_f32_e32 v2, v2, v38
	v_cndmask_b32_e32 v24, v1, v24, vcc
	v_lshlrev_b32_e32 v24, 2, v24
	ds_bpermute_b32 v24, v24, v2
	v_cvt_pk_bf16_f32 v28, v36, v37
	v_cvt_pk_bf16_f32 v29, v32, v33
	global_store_dwordx4 v[34:35], v[26:29], off offset:3072
	s_and_saveexec_b64 s[4:5], s[0:1]
	s_cbranch_execz .LBB0_2411
	s_waitcnt lgkmcnt(0)
	v_add_f32_e32 v2, v2, v24
	v_mul_f32_e32 v2, 0x4b800000, v2
	v_trunc_f32_e32 v2, v2
	v_mul_f32_e32 v24, 0x2f800000, v2
	v_floor_f32_e32 v25, v24
	v_fmac_f32_e32 v2, 0xcf800000, v25
	v_cvt_u32_f32_e32 v24, v2
	v_cvt_u32_f32_e32 v25, v25
	s_add_u32 s6, s52, s3
	s_addc_u32 s7, s53, s34
	global_store_dwordx2 v3, v[24:25], s[6:7]
	s_branch .LBB0_2411
